# speedup vs baseline: 1.0096x; 1.0096x over previous
.LBB0_3:
	s_load_dwordx2 s[8:9], s[0:1], 0x18
	s_load_dwordx2 s[4:5], s[0:1], 0x20
	s_add_i32 s3, s2, 0xfffffe00
	s_and_b32 s6, s3, 7
	s_lshr_b32 s7, s3, 3
	s_lshl_b32 s10, s7, 3
	s_sub_u32 s10, 0x441, s10
	v_cvt_f32_u32_e32 v1, s10
	v_sqrt_f32_e32 v1, v1
	v_and_b32_e32 v2, 7, v0
	v_bfe_u32 v3, v0, 3, 4
	v_sub_f32_e32 v1, 0x42040000, v1
	v_fmaak_f32 v1, 0.5, v1, 0x3c23d70a
	v_cvt_u32_f32_e32 v1, v1
	v_lshrrev_b32_e32 v4, 7, v0
	v_readfirstlane_b32 s11, v1
	v_lshlrev_b32_e32 v5, 19, v4
	v_lshl_or_b32 v5, v3, 11, v5
	v_lshl_or_b32 v5, v2, 4, v5
	s_sub_u32 s12, 33, s11
	s_mul_i32 s12, s12, s11
	s_lshr_b32 s12, s12, 1
	s_sub_u32 s13, s7, s12
	s_add_u32 s13, s13, s11
	s_cmp_lt_u32 s11, s13
	s_cselect_b32 s14, 1.0, 0
	s_mov_b32 s15, 0
	s_lshl_b32 s24, s6, 22
	s_lshl_b32 s16, s11, 15
	s_lshl_b32 s17, s13, 7
	s_add_u32 s16, s16, s17
	s_add_u32 s16, s16, s24
	s_lshl_b32 s18, s13, 15
	s_lshl_b32 s19, s11, 7
	s_add_u32 s18, s18, s19
	s_add_u32 s18, s18, s24
	s_waitcnt lgkmcnt(0)
	s_add_u32 s20, s8, s16
	s_addc_u32 s21, s9, 0
	s_add_u32 s22, s8, s18
	s_addc_u32 s23, s9, 0
	global_load_dwordx4 v[8:11], v5, s[20:21] nt
	global_load_dwordx4 v[12:15], v5, s[22:23] nt
	s_add_u32 s20, s20, 0x100000
	s_addc_u32 s21, s21, 0
	s_add_u32 s22, s22, 0x100000
	s_addc_u32 s23, s23, 0
	global_load_dwordx4 v[16:19], v5, s[20:21] nt
	global_load_dwordx4 v[20:23], v5, s[22:23] nt
	s_add_u32 s20, s20, 0x100000
	s_addc_u32 s21, s21, 0
	s_add_u32 s22, s22, 0x100000
	s_addc_u32 s23, s23, 0
	global_load_dwordx4 v[24:27], v5, s[20:21] nt
	global_load_dwordx4 v[28:31], v5, s[22:23] nt
	s_add_u32 s20, s20, 0x100000
	s_addc_u32 s21, s21, 0
	s_add_u32 s22, s22, 0x100000
	s_addc_u32 s23, s23, 0
	global_load_dwordx4 v[32:35], v5, s[20:21] nt
	global_load_dwordx4 v[36:39], v5, s[22:23] nt
	v_mul_u32_u24_e32 v6, 0x88, v3
	v_mul_u32_u24_e32 v7, 0x880, v4
	v_lshlrev_b32_e32 v40, 4, v2
	v_add3_u32 v6, v6, v7, v40
	v_mul_u32_u24_e32 v41, 0x110, v2
	v_lshlrev_b32_e32 v42, 3, v3
	v_add3_u32 v42, v7, v41, v42
	v_add_u32_e32 v42, 0x4400, v42
	v_add_u32_e32 v43, 0x1100, v6
	v_add_u32_e32 v44, 0x1100, v42
	v_add_u32_e32 v45, 0x2200, v6
	v_add_u32_e32 v46, 0x2200, v42
	v_add_u32_e32 v47, 0x3300, v6
	v_add_u32_e32 v48, 0x3300, v42
	v_and_b32_e32 v49, 15, v0
	v_bfe_u32 v50, v0, 4, 1
	v_lshrrev_b32_e32 v51, 5, v0
	v_mul_u32_u24_e32 v52, 0x880, v51
	v_mul_u32_u24_e32 v53, 0x88, v49
	v_lshlrev_b32_e32 v54, 6, v50
	v_add3_u32 v52, v52, v53, v54
	v_add_u32_e32 v53, 0x4400, v52
	v_lshlrev_b32_e32 v54, 9, v49
	v_lshl_or_b32 v54, v50, 7, v54
	v_lshl_or_b32 v54, v51, 4, v54
	s_waitcnt vmcnt(6)
	ds_write2_b64 v6, v[8:9], v[10:11] offset1:1
	ds_write2_b64 v42, v[12:13], v[14:15] offset1:17
	s_waitcnt vmcnt(4)
	ds_write2_b64 v43, v[16:17], v[18:19] offset1:1
	ds_write2_b64 v44, v[20:21], v[22:23] offset1:17
	s_waitcnt vmcnt(2)
	ds_write2_b64 v45, v[24:25], v[26:27] offset1:1
	ds_write2_b64 v46, v[28:29], v[30:31] offset1:17
	s_waitcnt vmcnt(0)
	ds_write2_b64 v47, v[32:33], v[34:35] offset1:1
	ds_write2_b64 v48, v[36:37], v[38:39] offset1:17
	s_waitcnt lgkmcnt(0)
	s_barrier
	ds_read2_b64 v[56:59], v52 offset0:0 offset1:1
	ds_read2_b64 v[60:63], v52 offset0:2 offset1:3
	ds_read2_b64 v[64:67], v52 offset0:4 offset1:5
	ds_read2_b64 v[68:71], v52 offset0:6 offset1:7
	ds_read2_b64 v[72:75], v53 offset0:0 offset1:1
	ds_read2_b64 v[76:79], v53 offset0:2 offset1:3
	ds_read2_b64 v[80:83], v53 offset0:4 offset1:5
	ds_read2_b64 v[84:87], v53 offset0:6 offset1:7
	v_lshlrev_b32_e32 v55, 4, v0
	v_lshlrev_b32_e32 v96, 12, v51
	v_lshl_or_b32 v96, v50, 11, v96
	v_and_b32_e32 v97, 1, v3
	v_lshl_or_b32 v96, v97, 9, v96
	v_lshl_or_b32 v96, v2, 4, v96
	s_lshl_b32 s25, s7, 16
	s_lshr_b32 s26, s6, 2
	s_lshl_b32 s26, s26, 10
	s_and_b32 s27, s6, 3
	s_lshl_b32 s27, s27, 7
	s_add_u32 s25, s25, s26
	s_add_u32 s25, s25, s27
	s_add_u32 s26, s4, s25
	s_addc_u32 s27, s5, 0
	s_add_u32 s28, s26, 0x8000
	s_addc_u32 s29, s27, 0
	s_waitcnt lgkmcnt(3)
	v_pk_fma_f32 v[56:57], s[14:15], v[72:73], v[56:57] op_sel_hi:[0,1,1] neg_hi:[0,0,1]
	v_pk_fma_f32 v[58:59], s[14:15], v[74:75], v[58:59] op_sel_hi:[0,1,1] neg_hi:[0,0,1]
	s_waitcnt lgkmcnt(2)
	v_pk_fma_f32 v[60:61], s[14:15], v[76:77], v[60:61] op_sel_hi:[0,1,1] neg_hi:[0,0,1]
	v_pk_fma_f32 v[62:63], s[14:15], v[78:79], v[62:63] op_sel_hi:[0,1,1] neg_hi:[0,0,1]
	s_waitcnt lgkmcnt(1)
	v_pk_fma_f32 v[64:65], s[14:15], v[80:81], v[64:65] op_sel_hi:[0,1,1] neg_hi:[0,0,1]
	v_pk_fma_f32 v[66:67], s[14:15], v[82:83], v[66:67] op_sel_hi:[0,1,1] neg_hi:[0,0,1]
	s_waitcnt lgkmcnt(0)
	v_pk_fma_f32 v[68:69], s[14:15], v[84:85], v[68:69] op_sel_hi:[0,1,1] neg_hi:[0,0,1]
	v_pk_fma_f32 v[70:71], s[14:15], v[86:87], v[70:71] op_sel_hi:[0,1,1] neg_hi:[0,0,1]
	v_cvt_pk_f16_f32 v88, v56, v58
	v_cvt_pk_f16_f32 v89, v60, v62
	v_cvt_pk_f16_f32 v90, v64, v66
	v_cvt_pk_f16_f32 v91, v68, v70
	v_cvt_pk_f16_f32 v92, v57, v59
	v_cvt_pk_f16_f32 v93, v61, v63
	v_cvt_pk_f16_f32 v94, v65, v67
	v_cvt_pk_f16_f32 v95, v69, v71
	ds_write_b128 v54, v[88:91] offset:34816
	ds_write_b128 v54, v[92:95] offset:35072
	s_waitcnt lgkmcnt(0)
	s_barrier
	ds_read_b128 v[8:11], v55 offset:34816
	ds_read_b128 v[12:15], v55 offset:38912
	s_waitcnt lgkmcnt(1)
	global_store_dwordx4 v96, v[8:11], s[26:27] sc0 sc1
	s_waitcnt lgkmcnt(0)
	global_store_dwordx4 v96, v[12:15], s[28:29] sc0 sc1
	s_endpgm
